# both GEMMs: whole prologue setup (LDS addresses, accumulator zeroing) runs before the first wait; the two prologue waits+barriers sit right before the loop
# speedup vs baseline: 1.0136x; 1.0023x over previous
.LBB5_2:
	s_or_b64 exec, exec, s[12:13]
	s_add_i32 s18, 0, 0x18000
	v_add_u32_e32 v60, s18, v18
	s_mov_b64 s[12:13], 0x100
	v_readfirstlane_b32 s19, v60
	v_add_u32_e32 v61, 0x2000, v60
	v_lshl_add_u64 v[2:3], v[2:3], 0, s[12:13]
	s_mov_b32 m0, s19
	v_readfirstlane_b32 s19, v61
	v_add_u32_e32 v62, 0x8000, v50
	global_load_lds_dwordx4 v[2:3], off
	v_lshl_add_u64 v[2:3], v[4:5], 0, s[12:13]
	s_mov_b32 m0, s19
	v_readfirstlane_b32 s19, v62
	v_add_u32_e32 v63, 0xa000, v50
	global_load_lds_dwordx4 v[2:3], off
	v_lshl_add_u64 v[2:3], v[6:7], 0, s[12:13]
	s_mov_b32 m0, s19
	v_readfirstlane_b32 s19, v63
	global_load_lds_dwordx4 v[2:3], off
	s_mov_b32 m0, s19
	s_add_i32 s19, 0, 0x1c000
	v_add_u32_e32 v64, s19, v18
	v_lshl_add_u64 v[2:3], v[8:9], 0, s[12:13]
	v_readfirstlane_b32 s20, v64
	global_load_lds_dwordx4 v[2:3], off
	v_lshl_add_u64 v[2:3], v[10:11], 0, s[12:13]
	s_mov_b32 m0, s20
	v_add_u32_e32 v66, 0x2000, v64
	global_load_lds_dwordx4 v[2:3], off
	v_lshl_add_u64 v[2:3], v[12:13], 0, s[12:13]
	v_readfirstlane_b32 s12, v66
	s_mov_b32 m0, s12
	v_lshlrev_b32_e32 v4, 2, v0
	global_load_lds_dwordx4 v[2:3], off
	v_lshlrev_b32_e32 v3, 6, v0
	v_and_b32_e32 v2, 48, v0
	v_and_b32_e32 v3, 0x3c0, v3
	v_and_b32_e32 v4, 32, v4
	s_and_b32 s12, s14, 7
	v_bitop3_b32 v2, v3, v4, v2 bitop3:0x36
	s_lshl_b32 s12, s12, 18
	s_load_dwordx2 s[0:1], s[0:1], 0x10
	s_mov_b32 s17, 0x18000
	v_add_u32_e32 v7, s15, v2
	v_add_u32_e32 v8, s16, v2
	v_add_u32_e32 v9, s18, v2
	v_add_u32_e32 v10, s19, v2
	v_add_u32_e32 v12, 0, v2
	v_lshlrev_b32_e32 v2, 3, v17
	v_lshlrev_b32_e32 v4, 11, v14
	s_add_u32 s4, s4, s12
	v_and_or_b32 v2, v2, s17, v4
	v_mov_b32_e32 v3, v39
	s_addc_u32 s5, s5, 0
	v_lshl_or_b32 v4, v1, 15, v4
	v_mov_b32_e32 v5, v39
	v_bfe_u32 v48, v0, 6, 2
	v_lshl_add_u64 v[40:41], s[4:5], 0, v[2:3]
	v_lshl_add_u64 v[42:43], s[4:5], 0, v[4:5]
	s_add_u32 s4, s6, s10
	v_lshlrev_b32_e32 v6, 12, v48
	v_lshlrev_b32_e32 v11, 13, v1
	s_addc_u32 s5, s7, s11
	v_lshrrev_b32_e32 v49, 2, v0
	v_add_u32_e32 v38, v15, v16
	v_lshl_add_u64 v[44:45], s[4:5], 0, v[2:3]
	v_lshl_add_u64 v[46:47], s[4:5], 0, v[4:5]
	s_mov_b32 s16, -2
	v_add_u32_e32 v67, v7, v6
	v_add_u32_e32 v52, v12, v11
	s_mov_b64 s[4:5], 0x20100
	v_add_u32_e32 v65, v8, v6
	s_mov_b64 s[6:7], 0x200
	s_mov_b64 s[10:11], 0x20200
	v_add_u32_e32 v59, v9, v6
	s_mov_b64 s[12:13], 0x300
	s_mov_b64 s[14:15], 0x20300
	v_add_u32_e32 v54, v10, v6
	v_mov_b32_e32 v2, v39
	v_mov_b32_e32 v4, v39
	v_mov_b32_e32 v6, v39
	v_mov_b32_e32 v7, v39
	v_mov_b32_e32 v8, v39
	v_mov_b32_e32 v9, v39
	v_mov_b32_e32 v10, v39
	v_mov_b32_e32 v11, v39
	v_mov_b32_e32 v12, v39
	v_mov_b32_e32 v13, v39
	v_mov_b32_e32 v14, v39
	v_mov_b32_e32 v15, v39
	v_mov_b32_e32 v16, v39
	v_mov_b32_e32 v17, v39
	v_mov_b32_e32 v18, v39
	v_mov_b32_e32 v19, v39
	v_mov_b32_e32 v20, v39
	v_mov_b32_e32 v21, v39
	v_mov_b32_e32 v22, v39
	v_mov_b32_e32 v23, v39
	v_mov_b32_e32 v24, v39
	v_mov_b32_e32 v25, v39
	v_mov_b32_e32 v26, v39
	v_mov_b32_e32 v27, v39
	v_mov_b32_e32 v28, v39
	v_mov_b32_e32 v29, v39
	v_mov_b32_e32 v30, v39
	v_mov_b32_e32 v31, v39
	v_mov_b32_e32 v32, v39
	v_mov_b32_e32 v33, v39
	v_add_u32_e32 v68, 0xc000, v50
	v_add_u32_e32 v69, 0xe000, v50
	v_add_u32_e32 v70, 0x2000, v51
	v_add_u32_e32 v71, 0x2000, v55
	s_waitcnt vmcnt(10)
	s_barrier
	s_waitcnt vmcnt(6)
	s_barrier

.LBB15_6:
	s_or_b64 exec, exec, s[8:9]
	s_add_i32 s27, 0, 0x18000
	v_add_u32_e32 v160, s27, v1
	s_load_dwordx4 s[8:11], s[0:1], 0x18
	s_mov_b64 s[0:1], 0x80
	v_readfirstlane_b32 s28, v160
	v_add_u32_e32 v161, 0x2000, v160
	v_lshl_add_u64 v[2:3], v[2:3], 0, s[0:1]
	s_mov_b32 m0, s28
	v_readfirstlane_b32 s28, v161
	v_add_u32_e32 v162, 0x8000, v153
	global_load_lds_dwordx4 v[2:3], off
	v_lshl_add_u64 v[2:3], v[4:5], 0, s[0:1]
	s_mov_b32 m0, s28
	v_readfirstlane_b32 s28, v162
	v_add_u32_e32 v163, 0xa000, v153
	global_load_lds_dwordx4 v[2:3], off
	v_lshl_add_u64 v[2:3], v[6:7], 0, s[0:1]
	s_mov_b32 m0, s28
	v_readfirstlane_b32 s28, v163
	global_load_lds_dwordx4 v[2:3], off
	s_mov_b32 m0, s28
	s_add_i32 s28, 0, 0x1c000
	v_add_u32_e32 v164, s28, v1
	v_lshl_add_u64 v[2:3], v[8:9], 0, s[0:1]
	v_readfirstlane_b32 s29, v164
	global_load_lds_dwordx4 v[2:3], off
	v_lshl_add_u64 v[2:3], v[10:11], 0, s[0:1]
	s_mov_b32 m0, s29
	v_add_u32_e32 v165, 0x2000, v164
	global_load_lds_dwordx4 v[2:3], off
	v_lshl_add_u64 v[2:3], v[12:13], 0, s[0:1]
	v_readfirstlane_b32 s0, v165
	s_mov_b32 m0, s0
	v_lshlrev_b32_e32 v4, 2, v0
	global_load_lds_dwordx4 v[2:3], off
	v_mov_b32_e32 v20, v131
	v_mov_b32_e32 v21, v131
	v_mov_b32_e32 v22, v131
	v_mov_b32_e32 v23, v131
	v_mov_b32_e32 v24, v131
	v_mov_b32_e32 v25, v131
	v_mov_b32_e32 v26, v131
	v_mov_b32_e32 v27, v131
	v_mov_b32_e32 v28, v131
	v_mov_b32_e32 v29, v131
	v_mov_b32_e32 v30, v131
	v_mov_b32_e32 v31, v131
	v_mov_b32_e32 v32, v131
	v_mov_b32_e32 v33, v131
	v_mov_b32_e32 v34, v131
	v_mov_b32_e32 v35, v131
	v_mov_b32_e32 v36, v131
	v_mov_b32_e32 v37, v131
	v_mov_b32_e32 v38, v131
	v_mov_b32_e32 v39, v131
	v_mov_b32_e32 v40, v131
	v_mov_b32_e32 v41, v131
	v_mov_b32_e32 v42, v131
	v_mov_b32_e32 v43, v131
	v_mov_b32_e32 v44, v131
	v_mov_b32_e32 v45, v131
	v_mov_b32_e32 v46, v131
	v_mov_b32_e32 v47, v131
	v_mov_b32_e32 v48, v131
	v_mov_b32_e32 v49, v131
	v_mov_b32_e32 v50, v131
	v_mov_b32_e32 v51, v131
	v_mov_b32_e32 v52, v131
	v_mov_b32_e32 v53, v131
	v_mov_b32_e32 v54, v131
	v_mov_b32_e32 v55, v131
	v_mov_b32_e32 v56, v131
	v_mov_b32_e32 v57, v131
	v_mov_b32_e32 v58, v131
	v_mov_b32_e32 v59, v131
	v_mov_b32_e32 v60, v131
	v_mov_b32_e32 v61, v131
	v_mov_b32_e32 v62, v131
	v_mov_b32_e32 v63, v131
	v_mov_b32_e32 v64, v131
	v_mov_b32_e32 v65, v131
	v_mov_b32_e32 v66, v131
	v_mov_b32_e32 v67, v131
	v_mov_b32_e32 v68, v131
	v_mov_b32_e32 v69, v131
	v_mov_b32_e32 v70, v131
	v_mov_b32_e32 v71, v131
	v_mov_b32_e32 v72, v131
	v_mov_b32_e32 v73, v131
	v_mov_b32_e32 v74, v131
	v_mov_b32_e32 v75, v131
	v_mov_b32_e32 v76, v131
	v_mov_b32_e32 v77, v131
	v_mov_b32_e32 v78, v131
	v_mov_b32_e32 v79, v131
	v_mov_b32_e32 v80, v131
	v_mov_b32_e32 v81, v131
	v_mov_b32_e32 v82, v131
	v_mov_b32_e32 v83, v131
	v_mov_b32_e32 v84, v131
	v_mov_b32_e32 v85, v131
	v_mov_b32_e32 v86, v131
	v_mov_b32_e32 v87, v131
	v_mov_b32_e32 v88, v131
	v_mov_b32_e32 v89, v131
	v_mov_b32_e32 v90, v131
	v_mov_b32_e32 v91, v131
	v_mov_b32_e32 v92, v131
	v_mov_b32_e32 v93, v131
	v_mov_b32_e32 v94, v131
	v_mov_b32_e32 v95, v131
	v_mov_b32_e32 v96, v131
	v_mov_b32_e32 v97, v131
	v_mov_b32_e32 v98, v131
	v_mov_b32_e32 v99, v131
	v_mov_b32_e32 v100, v131
	v_mov_b32_e32 v101, v131
	v_mov_b32_e32 v102, v131
	v_mov_b32_e32 v103, v131
	v_mov_b32_e32 v104, v131
	v_mov_b32_e32 v105, v131
	v_mov_b32_e32 v106, v131
	v_mov_b32_e32 v107, v131
	v_mov_b32_e32 v108, v131
	v_mov_b32_e32 v109, v131
	v_mov_b32_e32 v110, v131
	v_mov_b32_e32 v111, v131
	v_mov_b32_e32 v112, v131
	v_mov_b32_e32 v113, v131
	v_mov_b32_e32 v114, v131
	v_mov_b32_e32 v115, v131
	v_mov_b32_e32 v116, v131
	v_mov_b32_e32 v117, v131
	v_mov_b32_e32 v118, v131
	v_mov_b32_e32 v119, v131
	v_mov_b32_e32 v120, v131
	v_mov_b32_e32 v121, v131
	v_mov_b32_e32 v122, v131
	v_mov_b32_e32 v123, v131
	v_mov_b32_e32 v124, v131
	v_mov_b32_e32 v125, v131
	v_mov_b32_e32 v126, v131
	v_mov_b32_e32 v127, v131
	v_mov_b32_e32 v128, v131
	v_mov_b32_e32 v129, v131
	v_lshlrev_b32_e32 v3, 6, v0
	v_and_b32_e32 v2, 48, v0
	v_and_b32_e32 v3, 0x3c0, v3
	v_and_b32_e32 v4, 32, v4
	v_bitop3_b32 v2, v3, v4, v2 bitop3:0x36
	v_add_u32_e32 v7, s22, v2
	v_add_u32_e32 v8, s13, v2
	v_add_u32_e32 v9, s27, v2
	v_add_u32_e32 v10, s28, v2
	v_add_u32_e32 v12, 0, v2
	v_lshlrev_b32_e32 v2, 4, v17
	v_lshlrev_b32_e32 v4, 11, v14
	s_mov_b32 s0, 0x38000
	s_mov_b32 s26, 0x18000
	v_and_or_b32 v2, v2, s0, v4
	s_add_u32 s0, s23, s18
	v_lshlrev_b32_e32 v5, 8, v0
	v_mov_b32_e32 v3, v131
	s_addc_u32 s1, s7, s19
	v_and_or_b32 v4, v5, s26, v4
	v_mov_b32_e32 v5, v131
	v_bfe_u32 v147, v0, 6, 2
	v_lshlrev_b32_e32 v11, 13, v145
	v_lshl_add_u64 v[136:137], s[0:1], 0, v[2:3]
	v_lshl_add_u64 v[138:139], s[0:1], 0, v[4:5]
	s_add_u32 s0, s21, s2
	v_lshlrev_b32_e32 v6, 12, v147
	v_or_b32_e32 v13, 0x800, v11
	v_or_b32_e32 v18, 0x1000, v11
	v_or_b32_e32 v19, 0x1800, v11
	s_addc_u32 s1, s20, s3
	v_add_u32_e32 v130, v15, v16
	v_lshl_add_u64 v[140:141], s[0:1], 0, v[2:3]
	v_lshl_add_u64 v[142:143], s[0:1], 0, v[4:5]
	s_mov_b32 s7, -2
	v_add_u32_e32 v167, v7, v6
	v_add_u32_e32 v151, v12, v11
	v_add_u32_e32 v150, v12, v13
	v_add_u32_e32 v149, v12, v18
	v_add_u32_e32 v148, v12, v19
	s_mov_b64 s[0:1], 0x40080
	s_mov_b64 s[2:3], 0x100
	s_mov_b64 s[18:19], 0x40100
	s_mov_b64 s[20:21], 0x180
	s_mov_b64 s[22:23], 0x40180
	v_add_u32_e32 v166, v8, v6
	v_add_u32_e32 v157, v9, v6
	v_add_u32_e32 v154, v10, v6
	v_mov_b32_e32 v2, v131
	v_mov_b32_e32 v4, v131
	v_mov_b32_e32 v6, v131
	v_mov_b32_e32 v7, v131
	v_mov_b32_e32 v8, v131
	v_mov_b32_e32 v9, v131
	v_mov_b32_e32 v10, v131
	v_mov_b32_e32 v11, v131
	v_mov_b32_e32 v12, v131
	v_mov_b32_e32 v13, v131
	v_mov_b32_e32 v14, v131
	v_mov_b32_e32 v15, v131
	v_mov_b32_e32 v16, v131
	v_mov_b32_e32 v17, v131
	v_mov_b32_e32 v18, v131
	v_mov_b32_e32 v19, v131
	v_and_b32_e32 v144, 15, v0
	v_lshlrev_b32_e32 v146, 6, v145
	v_add_u32_e32 v168, 0xc000, v153
	v_add_u32_e32 v169, 0xe000, v153
	v_add_u32_e32 v170, 0x2000, v152
	v_add_u32_e32 v171, 0x2000, v156
	s_waitcnt vmcnt(10)
	s_barrier
	s_waitcnt vmcnt(6)
	s_barrier
